# layers 1-3: nodes of a 32-node tile paired by degree rank (largest with smallest) across the 16 lane-groups so every group and wave carries an equal edge count; self row added at pass end
# speedup vs baseline: 1.0034x; 1.0034x over previous
.Llay_fwd:
	v_lshrrev_b32_e32 v35, 3, v0
	s_lshl_b32 s24, s25, 5
	v_and_b32_e32 v60, 30, v35
	v_or_b32_e32 v8, s24, v60
	v_min_i32_e32 v2, 0x1869f, v8
	v_ashrrev_i32_e32 v3, 31, v2
	v_and_b32_e32 v1, 15, v0
	v_lshlrev_b64 v[2:3], 8, v[2:3]
	v_mov_b32_e32 v27, 0
	v_lshl_add_u64 v[2:3], s[4:5], 0, v[2:3]
	v_lshlrev_b32_e32 v26, 4, v1
	v_lshl_add_u64 v[2:3], v[2:3], 0, v[26:27]
	v_cmp_gt_u32_e32 vcc, 33, v0
	s_and_saveexec_b64 s[2:3], vcc
	s_cbranch_execz .LBB5_6
	v_add_u32_e32 v6, s24, v0
	v_min_i32_e32 v6, 0x186a0, v6
	v_ashrrev_i32_e32 v7, 31, v6
	v_lshl_add_u64 v[6:7], v[6:7], 2, s[8:9]
	global_load_dword v6, v[6:7], off
	v_lshlrev_b32_e32 v7, 2, v0
	s_waitcnt vmcnt(0)
	ds_write_b32 v7, v6 offset:12800
	ds_write_b32 v7, v0 offset:12944
.LBB5_6:
	s_or_b64 exec, exec, s[2:3]
	s_movk_i32 s2, 0x3000
	v_add_u32_e64 v6, s2, 0
	s_waitcnt lgkmcnt(0)
	s_barrier
	ds_read2_b32 v[28:29], v6 offset0:128 offset1:160
	s_load_dwordx2 s[8:9], s[0:1], 0x48
	s_load_dwordx2 s[10:11], s[0:1], 0x30
	s_waitcnt lgkmcnt(0)
	v_sub_u32_e32 v6, v29, v28
	v_cmp_gt_i32_e32 vcc, v6, v0
	s_and_saveexec_b64 s[2:3], vcc
	s_cbranch_execz .LBB5_9
	v_min_i32_e32 v9, 0x400, v6
	v_add_u32_e32 v6, v0, v28
	v_ashrrev_i32_e32 v7, 31, v6
	v_mov_b32_e32 v10, 0x2200
	v_lshl_add_u64 v[6:7], v[6:7], 2, s[14:15]
	v_lshl_add_u32 v10, v0, 2, v10
	s_mov_b64 s[6:7], 0
	s_mov_b64 s[12:13], 0x400
	v_mov_b32_e32 v11, v0
	s_mov_b32 s20, 1
.LBB5_8:
	global_load_dword v12, v[6:7], off
	s_cmp_eq_u32 s20, 1
	s_cbranch_scc0 .Ll1b_sort_skip
	s_mov_b32 s20, 0
	v_readfirstlane_b32 s21, v0
	s_cmp_lt_u32 s21, 64
	s_cbranch_scc0 .Ll1b_sort_skip
	s_mov_b64 s[22:23], exec
	s_mov_b32 exec_lo, -1
	s_mov_b32 exec_hi, 0
	v_lshlrev_b32_e32 v13, 2, v0
	v_add_u32_e32 v13, 0x3200, v13
	ds_read2_b32 v[14:15], v13 offset1:1
	s_waitcnt lgkmcnt(0)
	v_sub_u32_e32 v14, v15, v14
	v_lshl_or_b32 v14, v14, 5, v0
	v_mov_b32_e32 v15, 0
	v_readlane_b32 s21, v14, 0
	s_nop 1
	v_cmp_gt_u32_e32 vcc, s21, v14
	s_nop 1
	v_addc_co_u32_e32 v15, vcc, 0, v15, vcc
	v_readlane_b32 s21, v14, 1
	s_nop 1
	v_cmp_gt_u32_e32 vcc, s21, v14
	s_nop 1
	v_addc_co_u32_e32 v15, vcc, 0, v15, vcc
	v_readlane_b32 s21, v14, 2
	s_nop 1
	v_cmp_gt_u32_e32 vcc, s21, v14
	s_nop 1
	v_addc_co_u32_e32 v15, vcc, 0, v15, vcc
	v_readlane_b32 s21, v14, 3
	s_nop 1
	v_cmp_gt_u32_e32 vcc, s21, v14
	s_nop 1
	v_addc_co_u32_e32 v15, vcc, 0, v15, vcc
	v_readlane_b32 s21, v14, 4
	s_nop 1
	v_cmp_gt_u32_e32 vcc, s21, v14
	s_nop 1
	v_addc_co_u32_e32 v15, vcc, 0, v15, vcc
	v_readlane_b32 s21, v14, 5
	s_nop 1
	v_cmp_gt_u32_e32 vcc, s21, v14
	s_nop 1
	v_addc_co_u32_e32 v15, vcc, 0, v15, vcc
	v_readlane_b32 s21, v14, 6
	s_nop 1
	v_cmp_gt_u32_e32 vcc, s21, v14
	s_nop 1
	v_addc_co_u32_e32 v15, vcc, 0, v15, vcc
	v_readlane_b32 s21, v14, 7
	s_nop 1
	v_cmp_gt_u32_e32 vcc, s21, v14
	s_nop 1
	v_addc_co_u32_e32 v15, vcc, 0, v15, vcc
	v_readlane_b32 s21, v14, 8
	s_nop 1
	v_cmp_gt_u32_e32 vcc, s21, v14
	s_nop 1
	v_addc_co_u32_e32 v15, vcc, 0, v15, vcc
	v_readlane_b32 s21, v14, 9
	s_nop 1
	v_cmp_gt_u32_e32 vcc, s21, v14
	s_nop 1
	v_addc_co_u32_e32 v15, vcc, 0, v15, vcc
	v_readlane_b32 s21, v14, 10
	s_nop 1
	v_cmp_gt_u32_e32 vcc, s21, v14
	s_nop 1
	v_addc_co_u32_e32 v15, vcc, 0, v15, vcc
	v_readlane_b32 s21, v14, 11
	s_nop 1
	v_cmp_gt_u32_e32 vcc, s21, v14
	s_nop 1
	v_addc_co_u32_e32 v15, vcc, 0, v15, vcc
	v_readlane_b32 s21, v14, 12
	s_nop 1
	v_cmp_gt_u32_e32 vcc, s21, v14
	s_nop 1
	v_addc_co_u32_e32 v15, vcc, 0, v15, vcc
	v_readlane_b32 s21, v14, 13
	s_nop 1
	v_cmp_gt_u32_e32 vcc, s21, v14
	s_nop 1
	v_addc_co_u32_e32 v15, vcc, 0, v15, vcc
	v_readlane_b32 s21, v14, 14
	s_nop 1
	v_cmp_gt_u32_e32 vcc, s21, v14
	s_nop 1
	v_addc_co_u32_e32 v15, vcc, 0, v15, vcc
	v_readlane_b32 s21, v14, 15
	s_nop 1
	v_cmp_gt_u32_e32 vcc, s21, v14
	s_nop 1
	v_addc_co_u32_e32 v15, vcc, 0, v15, vcc
	v_readlane_b32 s21, v14, 16
	s_nop 1
	v_cmp_gt_u32_e32 vcc, s21, v14
	s_nop 1
	v_addc_co_u32_e32 v15, vcc, 0, v15, vcc
	v_readlane_b32 s21, v14, 17
	s_nop 1
	v_cmp_gt_u32_e32 vcc, s21, v14
	s_nop 1
	v_addc_co_u32_e32 v15, vcc, 0, v15, vcc
	v_readlane_b32 s21, v14, 18
	s_nop 1
	v_cmp_gt_u32_e32 vcc, s21, v14
	s_nop 1
	v_addc_co_u32_e32 v15, vcc, 0, v15, vcc
	v_readlane_b32 s21, v14, 19
	s_nop 1
	v_cmp_gt_u32_e32 vcc, s21, v14
	s_nop 1
	v_addc_co_u32_e32 v15, vcc, 0, v15, vcc
	v_readlane_b32 s21, v14, 20
	s_nop 1
	v_cmp_gt_u32_e32 vcc, s21, v14
	s_nop 1
	v_addc_co_u32_e32 v15, vcc, 0, v15, vcc
	v_readlane_b32 s21, v14, 21
	s_nop 1
	v_cmp_gt_u32_e32 vcc, s21, v14
	s_nop 1
	v_addc_co_u32_e32 v15, vcc, 0, v15, vcc
	v_readlane_b32 s21, v14, 22
	s_nop 1
	v_cmp_gt_u32_e32 vcc, s21, v14
	s_nop 1
	v_addc_co_u32_e32 v15, vcc, 0, v15, vcc
	v_readlane_b32 s21, v14, 23
	s_nop 1
	v_cmp_gt_u32_e32 vcc, s21, v14
	s_nop 1
	v_addc_co_u32_e32 v15, vcc, 0, v15, vcc
	v_readlane_b32 s21, v14, 24
	s_nop 1
	v_cmp_gt_u32_e32 vcc, s21, v14
	s_nop 1
	v_addc_co_u32_e32 v15, vcc, 0, v15, vcc
	v_readlane_b32 s21, v14, 25
	s_nop 1
	v_cmp_gt_u32_e32 vcc, s21, v14
	s_nop 1
	v_addc_co_u32_e32 v15, vcc, 0, v15, vcc
	v_readlane_b32 s21, v14, 26
	s_nop 1
	v_cmp_gt_u32_e32 vcc, s21, v14
	s_nop 1
	v_addc_co_u32_e32 v15, vcc, 0, v15, vcc
	v_readlane_b32 s21, v14, 27
	s_nop 1
	v_cmp_gt_u32_e32 vcc, s21, v14
	s_nop 1
	v_addc_co_u32_e32 v15, vcc, 0, v15, vcc
	v_readlane_b32 s21, v14, 28
	s_nop 1
	v_cmp_gt_u32_e32 vcc, s21, v14
	s_nop 1
	v_addc_co_u32_e32 v15, vcc, 0, v15, vcc
	v_readlane_b32 s21, v14, 29
	s_nop 1
	v_cmp_gt_u32_e32 vcc, s21, v14
	s_nop 1
	v_addc_co_u32_e32 v15, vcc, 0, v15, vcc
	v_readlane_b32 s21, v14, 30
	s_nop 1
	v_cmp_gt_u32_e32 vcc, s21, v14
	s_nop 1
	v_addc_co_u32_e32 v15, vcc, 0, v15, vcc
	v_readlane_b32 s21, v14, 31
	s_nop 1
	v_cmp_gt_u32_e32 vcc, s21, v14
	s_nop 1
	v_addc_co_u32_e32 v15, vcc, 0, v15, vcc
	v_lshlrev_b32_e32 v15, 2, v15
	ds_write_b32 v15, v0 offset:12944
	s_mov_b64 exec, s[22:23]
.Ll1b_sort_skip:
	v_add_u32_e32 v11, 0x100, v11
	v_cmp_ge_i32_e32 vcc, v11, v9
	v_lshl_add_u64 v[6:7], v[6:7], 0, s[12:13]
	s_or_b64 s[6:7], vcc, s[6:7]
	s_waitcnt vmcnt(0)
	ds_write_b32 v10, v12
	v_add_u32_e32 v10, 0x400, v10
	s_andn2_b64 exec, exec, s[6:7]
	s_cbranch_execnz .LBB5_8
.LBB5_9:
	s_or_b64 exec, exec, s[2:3]
	v_mov_b32_e32 v27, 0
	s_load_dwordx2 s[6:7], s[0:1], 0x40
	s_load_dwordx2 s[12:13], s[0:1], 0x10
	s_waitcnt lgkmcnt(0)
	s_barrier
	v_sub_u32_e32 v46, v29, v28
	v_cmp_gt_i32_e32 vcc, 0x401, v46
	s_cbranch_vccnz .Ll1b_fits
	global_load_dwordx4 v[2:5], v[2:3], off
	v_lshlrev_b32_e32 v7, 2, v60
	ds_read_b32 v6, v27 offset:12928
	ds_read_b64 v[44:45], v7 offset:12800
	s_mov_b32 s0, 0x186a0
	v_add_f32_e64 v34, s16, 1.0
	v_cmp_gt_i32_e32 vcc, s0, v8
	v_mov_b32_e32 v42, 0
	v_mov_b32_e32 v43, 0
	v_mov_b32_e32 v40, 0
	v_mov_b32_e32 v41, 0
	v_mov_b32_e32 v38, 0
	v_mov_b32_e32 v39, 0
	v_mov_b32_e32 v36, 0
	v_mov_b32_e32 v37, 0
	s_and_saveexec_b64 s[0:1], vcc
	s_cbranch_execz .LBB5_11
	s_waitcnt vmcnt(0)
	v_cvt_f32_f16_sdwa v9, v2 dst_sel:DWORD dst_unused:UNUSED_PAD src0_sel:WORD_1
	v_cvt_f32_f16_sdwa v11, v3 dst_sel:DWORD dst_unused:UNUSED_PAD src0_sel:WORD_1
	v_cvt_f32_f16_sdwa v13, v4 dst_sel:DWORD dst_unused:UNUSED_PAD src0_sel:WORD_1
	v_cvt_f32_f16_sdwa v15, v5 dst_sel:DWORD dst_unused:UNUSED_PAD src0_sel:WORD_1
	v_cvt_f32_f16_e32 v14, v5
	v_cvt_f32_f16_e32 v12, v4
	v_cvt_f32_f16_e32 v10, v3
	v_cvt_f32_f16_e32 v8, v2
	v_pk_mul_f32 v[36:37], v[34:35], v[14:15] op_sel_hi:[0,1]
	v_pk_mul_f32 v[38:39], v[34:35], v[12:13] op_sel_hi:[0,1]
	v_pk_mul_f32 v[40:41], v[34:35], v[10:11] op_sel_hi:[0,1]
	v_pk_mul_f32 v[42:43], v[34:35], v[8:9] op_sel_hi:[0,1]

.LBB5_24:
.Ll1b_fits:
	v_add_f32_e64 v34, s16, 1.0
	v_lshrrev_b32_e32 v46, 4, v0
	v_sub_u32_e32 v47, 31, v46
	v_lshlrev_b32_e32 v46, 2, v46
	v_lshlrev_b32_e32 v47, 2, v47
	ds_read_b32 v62, v46 offset:12944
	ds_read_b32 v63, v47 offset:12944
	s_mov_b64 s[22:23], exec
	s_movk_i32 s0, 0x2200
	s_waitcnt lgkmcnt(0)
	v_mov_b32_e32 v46, 0x3200
	v_lshl_add_u32 v46, v62, 2, v46
	ds_read2_b32 v[44:45], v46 offset1:1
	v_add_u32_e32 v47, s24, v62
	s_mov_b32 s2, 0x186a0
	v_cmp_gt_i32_e32 vcc, s2, v47
	s_mov_b64 s[14:15], vcc
	v_min_i32_e32 v47, 0x1869f, v47
	v_lshl_add_u32 v47, v47, 8, v26
	global_load_dwordx4 v[30:33], v47, s[4:5]
	v_mov_b32_e32 v36, 0
	v_mov_b32_e32 v37, 0
	v_mov_b32_e32 v38, 0
	v_mov_b32_e32 v39, 0
	v_mov_b32_e32 v40, 0
	v_mov_b32_e32 v41, 0
	v_mov_b32_e32 v42, 0
	v_mov_b32_e32 v43, 0
	s_waitcnt lgkmcnt(0)
	v_sub_u32_e32 v27, v44, v28
	v_lshl_add_u32 v27, v27, 2, s0
	v_lshl_add_u32 v29, v44, 8, v26
	v_cmp_lt_i32_e64 s[2:3], v44, v45
	v_add_u32_e32 v46, 1, v44
	v_cmp_lt_i32_e64 s[16:17], v46, v45
	v_add_u32_e32 v46, 2, v44
	v_cmp_lt_i32_e64 s[18:19], v46, v45
	v_add_u32_e32 v46, 3, v44
	v_cmp_lt_i32_e64 s[20:21], v46, v45
	s_mov_b64 exec, s[2:3]
	ds_read_b32 v2, v27 offset:0
	global_load_dwordx4 v[4:7], v29, s[12:13] offset:0
	s_waitcnt lgkmcnt(0)
	v_lshl_add_u32 v2, v2, 8, v26
	global_load_dwordx4 v[8:11], v2, s[4:5]
	ds_read_b32 v2, v27 offset:16
	s_mov_b64 exec, s[16:17]
	ds_read_b32 v3, v27 offset:4
	global_load_dwordx4 v[12:15], v29, s[12:13] offset:256
	s_waitcnt lgkmcnt(0)
	v_lshl_add_u32 v3, v3, 8, v26
	global_load_dwordx4 v[16:19], v3, s[4:5]
	ds_read_b32 v3, v27 offset:20
	s_mov_b64 exec, s[18:19]
	ds_read_b32 v24, v27 offset:8
	global_load_dwordx4 v[20:23], v29, s[12:13] offset:512
	s_waitcnt lgkmcnt(0)
	v_lshl_add_u32 v24, v24, 8, v26
	global_load_dwordx4 v[50:53], v24, s[4:5]
	ds_read_b32 v24, v27 offset:24
	s_mov_b64 exec, s[20:21]
	ds_read_b32 v25, v27 offset:12
	global_load_dwordx4 v[54:57], v29, s[12:13] offset:768
	s_waitcnt lgkmcnt(0)
	v_lshl_add_u32 v25, v25, 8, v26
	global_load_dwordx4 v[58:61], v25, s[4:5]
	ds_read_b32 v25, v27 offset:28
	s_mov_b64 exec, s[22:23]
	s_cmp_eq_u64 s[2:3], 0
	s_cbranch_scc1 .Ll1b_p1_empty

.Ll1b_p1_done:
	v_cvt_f32_f16_e32 v4, v30
	v_cvt_f32_f16_sdwa v5, v30 dst_sel:DWORD dst_unused:UNUSED_PAD src0_sel:WORD_1
	v_cvt_f32_f16_e32 v6, v31
	v_cvt_f32_f16_sdwa v7, v31 dst_sel:DWORD dst_unused:UNUSED_PAD src0_sel:WORD_1
	v_cvt_f32_f16_e32 v8, v32
	v_cvt_f32_f16_sdwa v9, v32 dst_sel:DWORD dst_unused:UNUSED_PAD src0_sel:WORD_1
	v_cvt_f32_f16_e32 v10, v33
	v_cvt_f32_f16_sdwa v11, v33 dst_sel:DWORD dst_unused:UNUSED_PAD src0_sel:WORD_1
	s_mov_b64 vcc, s[14:15]
	v_mul_f32_e32 v4, v34, v4
	v_mul_f32_e32 v5, v34, v5
	v_mul_f32_e32 v6, v34, v6
	v_mul_f32_e32 v7, v34, v7
	v_mul_f32_e32 v8, v34, v8
	v_mul_f32_e32 v9, v34, v9
	v_mul_f32_e32 v10, v34, v10
	v_mul_f32_e32 v11, v34, v11
	v_cndmask_b32_e32 v4, 0, v4, vcc
	v_cndmask_b32_e32 v5, 0, v5, vcc
	v_cndmask_b32_e32 v6, 0, v6, vcc
	v_cndmask_b32_e32 v7, 0, v7, vcc
	v_cndmask_b32_e32 v8, 0, v8, vcc
	v_cndmask_b32_e32 v9, 0, v9, vcc
	v_cndmask_b32_e32 v10, 0, v10, vcc
	v_cndmask_b32_e32 v11, 0, v11, vcc
	v_pk_add_f32 v[42:43], v[42:43], v[4:5]
	v_pk_add_f32 v[40:41], v[40:41], v[6:7]
	v_pk_add_f32 v[38:39], v[38:39], v[8:9]
	v_pk_add_f32 v[36:37], v[36:37], v[10:11]
	s_movk_i32 s2, 0x110
	v_cvt_pk_f16_f32 v5, v36, v37
	v_cvt_pk_f16_f32 v4, v38, v39
	v_cvt_pk_f16_f32 v3, v40, v41
	v_cvt_pk_f16_f32 v2, v42, v43
	v_mad_u32_u24 v46, v62, s2, v26
	ds_write_b128 v46, v[2:5]
	v_mov_b32_e32 v46, 0x3200
	v_lshl_add_u32 v46, v63, 2, v46
	ds_read2_b32 v[44:45], v46 offset1:1
	v_add_u32_e32 v47, s24, v63
	s_mov_b32 s2, 0x186a0
	v_cmp_gt_i32_e32 vcc, s2, v47
	s_mov_b64 s[14:15], vcc
	v_min_i32_e32 v47, 0x1869f, v47
	v_lshl_add_u32 v47, v47, 8, v26
	global_load_dwordx4 v[30:33], v47, s[4:5]
	v_mov_b32_e32 v36, 0
	v_mov_b32_e32 v37, 0
	v_mov_b32_e32 v38, 0
	v_mov_b32_e32 v39, 0
	v_mov_b32_e32 v40, 0
	v_mov_b32_e32 v41, 0
	v_mov_b32_e32 v42, 0
	v_mov_b32_e32 v43, 0
	s_waitcnt lgkmcnt(0)
	v_sub_u32_e32 v27, v44, v28
	v_lshl_add_u32 v27, v27, 2, s0
	v_lshl_add_u32 v29, v44, 8, v26
	v_cmp_lt_i32_e64 s[2:3], v44, v45
	v_add_u32_e32 v46, 1, v44
	v_cmp_lt_i32_e64 s[16:17], v46, v45
	v_add_u32_e32 v46, 2, v44
	v_cmp_lt_i32_e64 s[18:19], v46, v45
	v_add_u32_e32 v46, 3, v44
	v_cmp_lt_i32_e64 s[20:21], v46, v45
	s_mov_b64 exec, s[2:3]
	ds_read_b32 v2, v27 offset:0
	global_load_dwordx4 v[4:7], v29, s[12:13] offset:0
	s_waitcnt lgkmcnt(0)
	v_lshl_add_u32 v2, v2, 8, v26
	global_load_dwordx4 v[8:11], v2, s[4:5]
	ds_read_b32 v2, v27 offset:16
	s_mov_b64 exec, s[16:17]
	ds_read_b32 v3, v27 offset:4
	global_load_dwordx4 v[12:15], v29, s[12:13] offset:256
	s_waitcnt lgkmcnt(0)
	v_lshl_add_u32 v3, v3, 8, v26
	global_load_dwordx4 v[16:19], v3, s[4:5]
	ds_read_b32 v3, v27 offset:20
	s_mov_b64 exec, s[18:19]
	ds_read_b32 v24, v27 offset:8
	global_load_dwordx4 v[20:23], v29, s[12:13] offset:512
	s_waitcnt lgkmcnt(0)
	v_lshl_add_u32 v24, v24, 8, v26
	global_load_dwordx4 v[50:53], v24, s[4:5]
	ds_read_b32 v24, v27 offset:24
	s_mov_b64 exec, s[20:21]
	ds_read_b32 v25, v27 offset:12
	global_load_dwordx4 v[54:57], v29, s[12:13] offset:768
	s_waitcnt lgkmcnt(0)
	v_lshl_add_u32 v25, v25, 8, v26
	global_load_dwordx4 v[58:61], v25, s[4:5]
	ds_read_b32 v25, v27 offset:28
	s_mov_b64 exec, s[22:23]
	s_cmp_eq_u64 s[2:3], 0
	s_cbranch_scc1 .Ll1b_p2_empty

.Ll1b_p2_done:
	v_cvt_f32_f16_e32 v4, v30
	v_cvt_f32_f16_sdwa v5, v30 dst_sel:DWORD dst_unused:UNUSED_PAD src0_sel:WORD_1
	v_cvt_f32_f16_e32 v6, v31
	v_cvt_f32_f16_sdwa v7, v31 dst_sel:DWORD dst_unused:UNUSED_PAD src0_sel:WORD_1
	v_cvt_f32_f16_e32 v8, v32
	v_cvt_f32_f16_sdwa v9, v32 dst_sel:DWORD dst_unused:UNUSED_PAD src0_sel:WORD_1
	v_cvt_f32_f16_e32 v10, v33
	v_cvt_f32_f16_sdwa v11, v33 dst_sel:DWORD dst_unused:UNUSED_PAD src0_sel:WORD_1
	s_mov_b64 vcc, s[14:15]
	v_mul_f32_e32 v4, v34, v4
	v_mul_f32_e32 v5, v34, v5
	v_mul_f32_e32 v6, v34, v6
	v_mul_f32_e32 v7, v34, v7
	v_mul_f32_e32 v8, v34, v8
	v_mul_f32_e32 v9, v34, v9
	v_mul_f32_e32 v10, v34, v10
	v_mul_f32_e32 v11, v34, v11
	v_cndmask_b32_e32 v4, 0, v4, vcc
	v_cndmask_b32_e32 v5, 0, v5, vcc
	v_cndmask_b32_e32 v6, 0, v6, vcc
	v_cndmask_b32_e32 v7, 0, v7, vcc
	v_cndmask_b32_e32 v8, 0, v8, vcc
	v_cndmask_b32_e32 v9, 0, v9, vcc
	v_cndmask_b32_e32 v10, 0, v10, vcc
	v_cndmask_b32_e32 v11, 0, v11, vcc
	v_pk_add_f32 v[42:43], v[42:43], v[4:5]
	v_pk_add_f32 v[40:41], v[40:41], v[6:7]
	v_pk_add_f32 v[38:39], v[38:39], v[8:9]
	v_pk_add_f32 v[36:37], v[36:37], v[10:11]
	v_mov_b32_e32 v27, v63
	v_mov_b32_e32 v34, v42
	v_mov_b32_e32 v35, v43
	v_mov_b32_e32 v46, v40
	v_mov_b32_e32 v47, v41
	v_mov_b32_e32 v48, v38
	v_mov_b32_e32 v49, v39
	v_mov_b32_e32 v50, v36
	v_mov_b32_e32 v51, v37
	s_branch .LBB5_61

	.amdhsa_kernel _Z12layer_kernelILb0ELi256ELi32EEvPKDv8_DF16_PKfPS0_PiS6_S6_S2_S4_S5_PfPK15HIP_vector_typeIiLj2EEPKi
		.amdhsa_group_segment_fixed_size 13080
		.amdhsa_private_segment_fixed_size 0
		.amdhsa_kernarg_size 352
		.amdhsa_user_sgpr_count 2
		.amdhsa_user_sgpr_dispatch_ptr 0
		.amdhsa_user_sgpr_queue_ptr 0
		.amdhsa_user_sgpr_kernarg_segment_ptr 1
		.amdhsa_user_sgpr_dispatch_id 0
		.amdhsa_user_sgpr_kernarg_preload_length 0
		.amdhsa_user_sgpr_kernarg_preload_offset 0
		.amdhsa_user_sgpr_private_segment_size 0
		.amdhsa_uses_dynamic_stack 0
		.amdhsa_enable_private_segment 0
		.amdhsa_system_sgpr_workgroup_id_x 1
		.amdhsa_system_sgpr_workgroup_id_y 0
		.amdhsa_system_sgpr_workgroup_id_z 0
		.amdhsa_system_sgpr_workgroup_info 0
		.amdhsa_system_vgpr_workitem_id 0
		.amdhsa_next_free_vgpr 64
		.amdhsa_next_free_sgpr 30
		.amdhsa_accum_offset 64
		.amdhsa_reserve_vcc 1
		.amdhsa_float_round_mode_32 0
		.amdhsa_float_round_mode_16_64 0
		.amdhsa_float_denorm_mode_32 3
		.amdhsa_float_denorm_mode_16_64 3
		.amdhsa_dx10_clamp 1
		.amdhsa_ieee_mode 1
		.amdhsa_fp16_overflow 0
		.amdhsa_tg_split 0
		.amdhsa_exception_fp_ieee_invalid_op 0
		.amdhsa_exception_fp_denorm_src 0
		.amdhsa_exception_fp_ieee_div_zero 0
		.amdhsa_exception_fp_ieee_overflow 0
		.amdhsa_exception_fp_ieee_underflow 0
		.amdhsa_exception_fp_ieee_inexact 0
		.amdhsa_exception_int_div_zero 0
	.end_amdhsa_kernel

amdhsa.kernels:
  - .agpr_count:     0
    .args:
      - .actual_access:  read_only
        .address_space:  global
        .offset:         0
        .size:           8
        .value_kind:     global_buffer
      - .address_space:  global
        .offset:         8
        .size:           8
        .value_kind:     global_buffer
      - .actual_access:  read_only
        .address_space:  global
        .offset:         16
        .size:           8
        .value_kind:     global_buffer
      - .actual_access:  read_only
        .address_space:  global
        .offset:         24
        .size:           8
        .value_kind:     global_buffer
      - .actual_access:  write_only
        .address_space:  global
        .offset:         32
        .size:           8
        .value_kind:     global_buffer
      - .actual_access:  read_only
        .address_space:  global
        .offset:         40
        .size:           8
        .value_kind:     global_buffer
      - .actual_access:  write_only
        .address_space:  global
        .offset:         48
        .size:           8
        .value_kind:     global_buffer
      - .actual_access:  write_only
        .address_space:  global
        .offset:         56
        .size:           8
        .value_kind:     global_buffer
    .group_segment_fixed_size: 6400
    .kernarg_segment_align: 8
    .kernarg_segment_size: 64
    .language:       OpenCL C
    .language_version:
      - 2
      - 0
    .max_flat_workgroup_size: 1024
    .name:           _Z17prep_count_kernelPKfPDv8_DF16_S0_S0_S2_PKiPiP15HIP_vector_typeIfLj4EE
    .private_segment_fixed_size: 0
    .sgpr_count:     22
    .sgpr_spill_count: 0
    .symbol:         _Z17prep_count_kernelPKfPDv8_DF16_S0_S0_S2_PKiPiP15HIP_vector_typeIfLj4EE.kd
    .uniform_work_group_size: 1
    .uses_dynamic_stack: false
    .vgpr_count:     22
    .vgpr_spill_count: 0
    .wavefront_size: 64
  - .agpr_count:     0
    .args:
      - .actual_access:  read_only
        .address_space:  global
        .offset:         0
        .size:           8
        .value_kind:     global_buffer
      - .actual_access:  read_only
        .address_space:  global
        .offset:         8
        .size:           8
        .value_kind:     global_buffer
      - .actual_access:  read_only
        .address_space:  global
        .offset:         16
        .size:           8
        .value_kind:     global_buffer
      - .actual_access:  write_only
        .address_space:  global
        .offset:         24
        .size:           8
        .value_kind:     global_buffer
      - .actual_access:  write_only
        .address_space:  global
        .offset:         32
        .size:           8
        .value_kind:     global_buffer
    .group_segment_fixed_size: 124704
    .kernarg_segment_align: 8
    .kernarg_segment_size: 40
    .language:       OpenCL C
    .language_version:
      - 2
      - 0
    .max_flat_workgroup_size: 1024
    .name:           _Z14scatter_kernelPKiS0_S0_PiP15HIP_vector_typeIiLj2EE
    .private_segment_fixed_size: 0
    .sgpr_count:     55
    .sgpr_spill_count: 0
    .symbol:         _Z14scatter_kernelPKiS0_S0_PiP15HIP_vector_typeIiLj2EE.kd
    .uniform_work_group_size: 1
    .uses_dynamic_stack: false
    .vgpr_count:     128
    .vgpr_spill_count: 0
    .wavefront_size: 64
  - .agpr_count:     0
    .args:
      - .actual_access:  read_only
        .address_space:  global
        .offset:         0
        .size:           8
        .value_kind:     global_buffer
      - .address_space:  global
        .offset:         8
        .size:           8
        .value_kind:     global_buffer
      - .address_space:  global
        .offset:         16
        .size:           8
        .value_kind:     global_buffer
      - .actual_access:  read_only
        .address_space:  global
        .offset:         24
        .size:           8
        .value_kind:     global_buffer
      - .actual_access:  read_only
        .address_space:  global
        .offset:         32
        .size:           8
        .value_kind:     global_buffer
      - .actual_access:  read_only
        .address_space:  global
        .offset:         40
        .size:           8
        .value_kind:     global_buffer
      - .offset:         48
        .size:           4
        .value_kind:     hidden_block_count_x
      - .offset:         52
        .size:           4
        .value_kind:     hidden_block_count_y
      - .offset:         56
        .size:           4
        .value_kind:     hidden_block_count_z
      - .offset:         60
        .size:           2
        .value_kind:     hidden_group_size_x
      - .offset:         62
        .size:           2
        .value_kind:     hidden_group_size_y
      - .offset:         64
        .size:           2
        .value_kind:     hidden_group_size_z
      - .offset:         66
        .size:           2
        .value_kind:     hidden_remainder_x
      - .offset:         68
        .size:           2
        .value_kind:     hidden_remainder_y
      - .offset:         70
        .size:           2
        .value_kind:     hidden_remainder_z
      - .offset:         88
        .size:           8
        .value_kind:     hidden_global_offset_x
      - .offset:         96
        .size:           8
        .value_kind:     hidden_global_offset_y
      - .offset:         104
        .size:           8
        .value_kind:     hidden_global_offset_z
      - .offset:         112
        .size:           2
        .value_kind:     hidden_grid_dims
    .group_segment_fixed_size: 1024
    .kernarg_segment_align: 8
    .kernarg_segment_size: 304
    .language:       OpenCL C
    .language_version:
      - 2
      - 0
    .max_flat_workgroup_size: 256
    .name:           _Z9bn_kernelPKDv8_DF16_S1_PS_PKfS4_S4_
    .private_segment_fixed_size: 0
    .sgpr_count:     20
    .sgpr_spill_count: 0
    .symbol:         _Z9bn_kernelPKDv8_DF16_S1_PS_PKfS4_S4_.kd
    .uniform_work_group_size: 1
    .uses_dynamic_stack: false
    .vgpr_count:     64
    .vgpr_spill_count: 0
    .wavefront_size: 64
  - .agpr_count:     0
    .args:
      - .actual_access:  read_only
        .address_space:  global
        .offset:         0
        .size:           8
        .value_kind:     global_buffer
      - .actual_access:  read_only
        .address_space:  global
        .offset:         8
        .size:           8
        .value_kind:     global_buffer
      - .actual_access:  read_only
        .address_space:  global
        .offset:         16
        .size:           8
        .value_kind:     global_buffer
      - .actual_access:  read_only
        .address_space:  global
        .offset:         24
        .size:           8
        .value_kind:     global_buffer
      - .actual_access:  read_only
        .address_space:  global
        .offset:         32
        .size:           8
        .value_kind:     global_buffer
      - .actual_access:  read_only
        .address_space:  global
        .offset:         40
        .size:           8
        .value_kind:     global_buffer
      - .actual_access:  read_only
        .address_space:  global
        .offset:         48
        .size:           8
        .value_kind:     global_buffer
      - .actual_access:  write_only
        .address_space:  global
        .offset:         56
        .size:           8
        .value_kind:     global_buffer
      - .offset:         64
        .size:           4
        .value_kind:     hidden_block_count_x
      - .offset:         68
        .size:           4
        .value_kind:     hidden_block_count_y
      - .offset:         72
        .size:           4
        .value_kind:     hidden_block_count_z
      - .offset:         76
        .size:           2
        .value_kind:     hidden_group_size_x
      - .offset:         78
        .size:           2
        .value_kind:     hidden_group_size_y
      - .offset:         80
        .size:           2
        .value_kind:     hidden_group_size_z
      - .offset:         82
        .size:           2
        .value_kind:     hidden_remainder_x
      - .offset:         84
        .size:           2
        .value_kind:     hidden_remainder_y
      - .offset:         86
        .size:           2
        .value_kind:     hidden_remainder_z
      - .offset:         104
        .size:           8
        .value_kind:     hidden_global_offset_x
      - .offset:         112
        .size:           8
        .value_kind:     hidden_global_offset_y
      - .offset:         120
        .size:           8
        .value_kind:     hidden_global_offset_z
      - .offset:         128
        .size:           2
        .value_kind:     hidden_grid_dims
    .group_segment_fixed_size: 34816
    .kernarg_segment_align: 8
    .kernarg_segment_size: 320
    .language:       OpenCL C
    .language_version:
      - 2
      - 0
    .max_flat_workgroup_size: 512
    .name:           _Z12final_kernelPKDv8_DF16_S1_PKfS3_S3_S1_S3_Pf
    .private_segment_fixed_size: 0
    .sgpr_count:     34
    .sgpr_spill_count: 0
    .symbol:         _Z12final_kernelPKDv8_DF16_S1_PKfS3_S3_S1_S3_Pf.kd
    .uniform_work_group_size: 1
    .uses_dynamic_stack: false
    .vgpr_count:     60
    .vgpr_spill_count: 0
    .wavefront_size: 64
  - .agpr_count:     0
    .args:
      - .actual_access:  read_only
        .address_space:  global
        .offset:         0
        .size:           8
        .value_kind:     global_buffer
      - .actual_access:  read_only
        .address_space:  global
        .offset:         8
        .size:           8
        .value_kind:     global_buffer
      - .address_space:  global
        .offset:         16
        .size:           8
        .value_kind:     global_buffer
      - .actual_access:  write_only
        .address_space:  global
        .offset:         24
        .size:           8
        .value_kind:     global_buffer
      - .address_space:  global
        .offset:         32
        .size:           8
        .value_kind:     global_buffer
      - .address_space:  global
        .offset:         40
        .size:           8
        .value_kind:     global_buffer
      - .actual_access:  read_only
        .address_space:  global
        .offset:         48
        .size:           8
        .value_kind:     global_buffer
      - .actual_access:  read_only
        .address_space:  global
        .offset:         56
        .size:           8
        .value_kind:     global_buffer
      - .address_space:  global
        .offset:         64
        .size:           8
        .value_kind:     global_buffer
      - .address_space:  global
        .offset:         72
        .size:           8
        .value_kind:     global_buffer
      - .actual_access:  read_only
        .address_space:  global
        .offset:         80
        .size:           8
        .value_kind:     global_buffer
      - .actual_access:  read_only
        .address_space:  global
        .offset:         88
        .size:           8
        .value_kind:     global_buffer
      - .offset:         96
        .size:           4
        .value_kind:     hidden_block_count_x
      - .offset:         100
        .size:           4
        .value_kind:     hidden_block_count_y
      - .offset:         104
        .size:           4
        .value_kind:     hidden_block_count_z
      - .offset:         108
        .size:           2
        .value_kind:     hidden_group_size_x
      - .offset:         110
        .size:           2
        .value_kind:     hidden_group_size_y
      - .offset:         112
        .size:           2
        .value_kind:     hidden_group_size_z
      - .offset:         114
        .size:           2
        .value_kind:     hidden_remainder_x
      - .offset:         116
        .size:           2
        .value_kind:     hidden_remainder_y
      - .offset:         118
        .size:           2
        .value_kind:     hidden_remainder_z
      - .offset:         136
        .size:           8
        .value_kind:     hidden_global_offset_x
      - .offset:         144
        .size:           8
        .value_kind:     hidden_global_offset_y
      - .offset:         152
        .size:           8
        .value_kind:     hidden_global_offset_z
      - .offset:         160
        .size:           2
        .value_kind:     hidden_grid_dims
    .group_segment_fixed_size: 26384
    .kernarg_segment_align: 8
    .kernarg_segment_size: 352
    .language:       OpenCL C
    .language_version:
      - 2
      - 0
    .max_flat_workgroup_size: 512
    .name:           _Z12layer_kernelILb1ELi512ELi64EEvPKDv8_DF16_PKfPS0_PiS6_S6_S2_S4_S5_PfPK15HIP_vector_typeIiLj2EEPKi
    .private_segment_fixed_size: 0
    .sgpr_count:     52
    .sgpr_spill_count: 0
    .symbol:         _Z12layer_kernelILb1ELi512ELi64EEvPKDv8_DF16_PKfPS0_PiS6_S6_S2_S4_S5_PfPK15HIP_vector_typeIiLj2EEPKi.kd
    .uniform_work_group_size: 1
    .uses_dynamic_stack: false
    .vgpr_count:     61
    .vgpr_spill_count: 0
    .wavefront_size: 64
  - .agpr_count:     0
    .args:
      - .actual_access:  read_only
        .address_space:  global
        .offset:         0
        .size:           8
        .value_kind:     global_buffer
      - .actual_access:  read_only
        .address_space:  global
        .offset:         8
        .size:           8
        .value_kind:     global_buffer
      - .actual_access:  read_only
        .address_space:  global
        .offset:         16
        .size:           8
        .value_kind:     global_buffer
      - .actual_access:  read_only
        .address_space:  global
        .offset:         24
        .size:           8
        .value_kind:     global_buffer
      - .actual_access:  read_only
        .address_space:  global
        .offset:         32
        .size:           8
        .value_kind:     global_buffer
      - .actual_access:  read_only
        .address_space:  global
        .offset:         40
        .size:           8
        .value_kind:     global_buffer
      - .actual_access:  read_only
        .address_space:  global
        .offset:         48
        .size:           8
        .value_kind:     global_buffer
      - .actual_access:  read_only
        .address_space:  global
        .offset:         56
        .size:           8
        .value_kind:     global_buffer
      - .address_space:  global
        .offset:         64
        .size:           8
        .value_kind:     global_buffer
      - .address_space:  global
        .offset:         72
        .size:           8
        .value_kind:     global_buffer
      - .actual_access:  read_only
        .address_space:  global
        .offset:         80
        .size:           8
        .value_kind:     global_buffer
      - .actual_access:  read_only
        .address_space:  global
        .offset:         88
        .size:           8
        .value_kind:     global_buffer
      - .offset:         96
        .size:           4
        .value_kind:     hidden_block_count_x
      - .offset:         100
        .size:           4
        .value_kind:     hidden_block_count_y
      - .offset:         104
        .size:           4
        .value_kind:     hidden_block_count_z
      - .offset:         108
        .size:           2
        .value_kind:     hidden_group_size_x
      - .offset:         110
        .size:           2
        .value_kind:     hidden_group_size_y
      - .offset:         112
        .size:           2
        .value_kind:     hidden_group_size_z
      - .offset:         114
        .size:           2
        .value_kind:     hidden_remainder_x
      - .offset:         116
        .size:           2
        .value_kind:     hidden_remainder_y
      - .offset:         118
        .size:           2
        .value_kind:     hidden_remainder_z
      - .offset:         136
        .size:           8
        .value_kind:     hidden_global_offset_x
      - .offset:         144
        .size:           8
        .value_kind:     hidden_global_offset_y
      - .offset:         152
        .size:           8
        .value_kind:     hidden_global_offset_z
      - .offset:         160
        .size:           2
        .value_kind:     hidden_grid_dims
    .group_segment_fixed_size: 13080
    .kernarg_segment_align: 8
    .kernarg_segment_size: 352
    .language:       OpenCL C
    .language_version:
      - 2
      - 0
    .max_flat_workgroup_size: 256
    .name:           _Z12layer_kernelILb0ELi256ELi32EEvPKDv8_DF16_PKfPS0_PiS6_S6_S2_S4_S5_PfPK15HIP_vector_typeIiLj2EEPKi
    .private_segment_fixed_size: 0
    .sgpr_count:     36
    .sgpr_spill_count: 0
    .symbol:         _Z12layer_kernelILb0ELi256ELi32EEvPKDv8_DF16_PKfPS0_PiS6_S6_S2_S4_S5_PfPK15HIP_vector_typeIiLj2EEPKi.kd
    .uniform_work_group_size: 1
    .uses_dynamic_stack: false
    .vgpr_count:     64
    .vgpr_spill_count: 0
    .wavefront_size: 64
